# P7 MoE down-GEMM unit loop: ticket of the dynamic tail drawn one unit ahead (atomic issued before the epilogue), on top of v5
# speedup vs baseline: 1.0015x; 1.0015x over previous
.LBB0_2490:
	s_add_i32 s80, s69, 1
	s_mov_b64 s[4:5], 0
	s_cmp_ge_i32 s80, s72
	s_mov_b64 s[6:7], -1
	s_cbranch_scc0 .LBB0_2499
	s_and_saveexec_b64 s[4:5], s[0:1]
	s_xor_b64 s[4:5], exec, s[4:5]
	s_and_b32 s6, s80, 1
	s_or_saveexec_b64 s[4:5], s[4:5]
	v_mov_b32_e32 v2, s6
	s_xor_b64 exec, exec, s[4:5]
	s_cbranch_execz .LBB0_2497
	s_mov_b64 s[8:9], exec
	v_mbcnt_lo_u32_b32 v2, s8, 0
	v_mbcnt_hi_u32_b32 v2, s9, v2
	v_cmp_eq_u32_e32 vcc, 0, v2
	s_and_saveexec_b64 s[6:7], vcc
	s_cbranch_execz .LBB0_2496
	s_bcnt1_i32_b64 s8, s[8:9]
	v_mov_b32_e32 v3, s8
	s_cmp_lg_u32 s69, 0
	s_cbranch_scc1 .Lp7_tk_have
	global_atomic_add v3, v195, v3, s[36:37] offset:2080 sc0
	s_branch .LBB0_2496
.Lp7_tk_have:
	s_waitcnt vmcnt(0)
	v_mov_b32_e32 v3, v254

.LBB0_2556:
	s_cmp_lg_u64 s[48:49], 0
	s_cbranch_scc1 .Lp7_tk_skip
	s_add_i32 s10, s80, 1
	s_cmp_lt_i32 s10, s72
	s_cbranch_scc1 .Lp7_tk_skip
	s_mov_b64 s[10:11], exec
	s_andn2_b64 exec, exec, s[0:1]
	s_cbranch_execz .Lp7_tk_rest
	v_mov_b32_e32 v254, 1
	global_atomic_add v254, v195, v254, s[36:37] offset:2080 sc0
.Lp7_tk_rest:
	s_mov_b64 exec, s[10:11]

	.amdhsa_kernel _Z10fwd_kernel4Args
		.amdhsa_group_segment_fixed_size 0
		.amdhsa_private_segment_fixed_size 0
		.amdhsa_kernarg_size 424
		.amdhsa_user_sgpr_count 2
		.amdhsa_user_sgpr_dispatch_ptr 0
		.amdhsa_user_sgpr_queue_ptr 0
		.amdhsa_user_sgpr_kernarg_segment_ptr 1
		.amdhsa_user_sgpr_dispatch_id 0
		.amdhsa_user_sgpr_kernarg_preload_length 0
		.amdhsa_user_sgpr_kernarg_preload_offset 0
		.amdhsa_user_sgpr_private_segment_size 0
		.amdhsa_uses_dynamic_stack 0
		.amdhsa_enable_private_segment 0
		.amdhsa_system_sgpr_workgroup_id_x 1
		.amdhsa_system_sgpr_workgroup_id_y 0
		.amdhsa_system_sgpr_workgroup_id_z 0
		.amdhsa_system_sgpr_workgroup_info 0
		.amdhsa_system_vgpr_workitem_id 0
		.amdhsa_next_free_vgpr 255
		.amdhsa_next_free_sgpr 100
		.amdhsa_accum_offset 256
		.amdhsa_reserve_vcc 1
		.amdhsa_float_round_mode_32 0
		.amdhsa_float_round_mode_16_64 0
		.amdhsa_float_denorm_mode_32 3
		.amdhsa_float_denorm_mode_16_64 3
		.amdhsa_dx10_clamp 1
		.amdhsa_ieee_mode 1
		.amdhsa_fp16_overflow 0
		.amdhsa_tg_split 0
		.amdhsa_exception_fp_ieee_invalid_op 0
		.amdhsa_exception_fp_denorm_src 0
		.amdhsa_exception_fp_ieee_div_zero 0
		.amdhsa_exception_fp_ieee_overflow 0
		.amdhsa_exception_fp_ieee_underflow 0
		.amdhsa_exception_fp_ieee_inexact 0
		.amdhsa_exception_int_div_zero 0
	.end_amdhsa_kernel

.Lfunc_end0:
	.size	_Z10fwd_kernel4Args, .Lfunc_end0-_Z10fwd_kernel4Args
	.set _Z10fwd_kernel4Args.num_vgpr, 255
	.set _Z10fwd_kernel4Args.num_agpr, 0
	.set _Z10fwd_kernel4Args.numbered_sgpr, 100
	.set _Z10fwd_kernel4Args.num_named_barrier, 0
	.set _Z10fwd_kernel4Args.private_seg_size, 0
	.set _Z10fwd_kernel4Args.uses_vcc, 1
	.set _Z10fwd_kernel4Args.uses_flat_scratch, 0
	.set _Z10fwd_kernel4Args.has_dyn_sized_stack, 0
	.set _Z10fwd_kernel4Args.has_recursion, 0
	.set _Z10fwd_kernel4Args.has_indirect_call, 0

amdhsa.kernels:
  - .agpr_count:     0
    .args:
      - .offset:         0
        .size:           168
        .value_kind:     by_value
      - .offset:         168
        .size:           4
        .value_kind:     hidden_block_count_x
      - .offset:         172
        .size:           4
        .value_kind:     hidden_block_count_y
      - .offset:         176
        .size:           4
        .value_kind:     hidden_block_count_z
      - .offset:         180
        .size:           2
        .value_kind:     hidden_group_size_x
      - .offset:         182
        .size:           2
        .value_kind:     hidden_group_size_y
      - .offset:         184
        .size:           2
        .value_kind:     hidden_group_size_z
      - .offset:         186
        .size:           2
        .value_kind:     hidden_remainder_x
      - .offset:         188
        .size:           2
        .value_kind:     hidden_remainder_y
      - .offset:         190
        .size:           2
        .value_kind:     hidden_remainder_z
      - .offset:         208
        .size:           8
        .value_kind:     hidden_global_offset_x
      - .offset:         216
        .size:           8
        .value_kind:     hidden_global_offset_y
      - .offset:         224
        .size:           8
        .value_kind:     hidden_global_offset_z
      - .offset:         232
        .size:           2
        .value_kind:     hidden_grid_dims
      - .offset:         288
        .size:           4
        .value_kind:     hidden_dynamic_lds_size
    .group_segment_fixed_size: 0
    .kernarg_segment_align: 8
    .kernarg_segment_size: 424
    .language:       OpenCL C
    .language_version:
      - 2
      - 0
    .max_flat_workgroup_size: 512
    .name:           _Z10fwd_kernel4Args
    .private_segment_fixed_size: 0
    .sgpr_count:     106
    .sgpr_spill_count: 157
    .symbol:         _Z10fwd_kernel4Args.kd
    .uniform_work_group_size: 1
    .uses_dynamic_stack: false
    .vgpr_count:     255
    .vgpr_spill_count: 0
    .wavefront_size: 64
